# hand-written K1: 8-deep 1KiB nt load ring per wave (fewer bytes in flight than ring-32), LDS queue counted in SGPRs, one batched slot-atomic round trip at wave end, pipelined f32-MFMA GEMM
# speedup vs baseline: 1.0639x; 1.0639x over previous
.Lk1_scan:
	s_load_dwordx2 s[4:5], s[0:1], 0x0
	s_load_dwordx4 s[8:11], s[0:1], 0x20
	s_load_dwordx2 s[12:13], s[0:1], 0x30
	v_and_b32_e32 v6, 63, v0
	v_readfirstlane_b32 s3, v0
	v_lshlrev_b32_e32 v1, 4, v6
	v_lshlrev_b32_e32 v2, 2, v6
	v_or_b32_e32 v3, 1, v2
	v_or_b32_e32 v4, 2, v2
	v_or_b32_e32 v5, 3, v2
	s_lshr_b32 s3, s3, 6
	s_sub_u32 s16, s2, 0x60
	s_lshl_b32 s16, s16, 2
	s_add_u32 s16, s16, s3
	s_mul_i32 s17, s16, 0x48000
	s_lshr_b32 s18, s17, 2
	s_lshl_b32 s24, s3, 13
	s_mov_b32 s25, s24
	s_mov_b32 s28, s24
	s_mov_b32 s36, 0
	v_mov_b32_e32 v21, 1
	s_mov_b32 s27, 0
	s_mov_b32 s29, 0x55555556
	s_mov_b32 s31, 0xc0000
	s_waitcnt lgkmcnt(0)
	s_add_u32 s6, s4, s17
	s_addc_u32 s7, s5, 0
	global_load_dwordx4 v[28:31], v1, s[6:7] nt
	s_add_u32 s6, s6, 0x400
	s_addc_u32 s7, s7, 0
	global_load_dwordx4 v[32:35], v1, s[6:7] nt
	s_add_u32 s6, s6, 0x400
	s_addc_u32 s7, s7, 0
	global_load_dwordx4 v[36:39], v1, s[6:7] nt
	s_add_u32 s6, s6, 0x400
	s_addc_u32 s7, s7, 0
	global_load_dwordx4 v[40:43], v1, s[6:7] nt
	s_add_u32 s6, s6, 0x400
	s_addc_u32 s7, s7, 0
	global_load_dwordx4 v[44:47], v1, s[6:7] nt
	s_add_u32 s6, s6, 0x400
	s_addc_u32 s7, s7, 0
	global_load_dwordx4 v[48:51], v1, s[6:7] nt
	s_add_u32 s6, s6, 0x400
	s_addc_u32 s7, s7, 0
	global_load_dwordx4 v[52:55], v1, s[6:7] nt
	s_add_u32 s6, s6, 0x400
	s_addc_u32 s7, s7, 0
	global_load_dwordx4 v[56:59], v1, s[6:7] nt
	s_add_u32 s6, s6, 0x400
	s_addc_u32 s7, s7, 0
	s_mov_b32 s26, 36
.Lk1_main:
	s_waitcnt vmcnt(7)
	v_or3_b32 v12, v28, v29, v30
	v_or_b32_e32 v12, v12, v31
	v_cmp_ne_u32_e32 vcc, 0, v12
	s_cbranch_vccnz .Lk1_hitm_0
.Lk1_contm_0:
	global_load_dwordx4 v[28:31], v1, s[6:7] nt
	s_add_u32 s6, s6, 0x400
	s_addc_u32 s7, s7, 0
	s_waitcnt vmcnt(7)
	v_or3_b32 v12, v32, v33, v34
	v_or_b32_e32 v12, v12, v35
	v_cmp_ne_u32_e32 vcc, 0, v12
	s_cbranch_vccnz .Lk1_hitm_1
.Lk1_contm_1:
	global_load_dwordx4 v[32:35], v1, s[6:7] nt
	s_add_u32 s6, s6, 0x400
	s_addc_u32 s7, s7, 0
	s_waitcnt vmcnt(7)
	v_or3_b32 v12, v36, v37, v38
	v_or_b32_e32 v12, v12, v39
	v_cmp_ne_u32_e32 vcc, 0, v12
	s_cbranch_vccnz .Lk1_hitm_2
.Lk1_contm_2:
	global_load_dwordx4 v[36:39], v1, s[6:7] nt
	s_add_u32 s6, s6, 0x400
	s_addc_u32 s7, s7, 0
	s_waitcnt vmcnt(7)
	v_or3_b32 v12, v40, v41, v42
	v_or_b32_e32 v12, v12, v43
	v_cmp_ne_u32_e32 vcc, 0, v12
	s_cbranch_vccnz .Lk1_hitm_3
.Lk1_contm_3:
	global_load_dwordx4 v[40:43], v1, s[6:7] nt
	s_add_u32 s6, s6, 0x400
	s_addc_u32 s7, s7, 0
	s_waitcnt vmcnt(7)
	v_or3_b32 v12, v44, v45, v46
	v_or_b32_e32 v12, v12, v47
	v_cmp_ne_u32_e32 vcc, 0, v12
	s_cbranch_vccnz .Lk1_hitm_4
.Lk1_contm_4:
	global_load_dwordx4 v[44:47], v1, s[6:7] nt
	s_add_u32 s6, s6, 0x400
	s_addc_u32 s7, s7, 0
	s_waitcnt vmcnt(7)
	v_or3_b32 v12, v48, v49, v50
	v_or_b32_e32 v12, v12, v51
	v_cmp_ne_u32_e32 vcc, 0, v12
	s_cbranch_vccnz .Lk1_hitm_5
.Lk1_contm_5:
	global_load_dwordx4 v[48:51], v1, s[6:7] nt
	s_add_u32 s6, s6, 0x400
	s_addc_u32 s7, s7, 0
	s_waitcnt vmcnt(7)
	v_or3_b32 v12, v52, v53, v54
	v_or_b32_e32 v12, v12, v55
	v_cmp_ne_u32_e32 vcc, 0, v12
	s_cbranch_vccnz .Lk1_hitm_6
.Lk1_contm_6:
	global_load_dwordx4 v[52:55], v1, s[6:7] nt
	s_add_u32 s6, s6, 0x400
	s_addc_u32 s7, s7, 0
	s_waitcnt vmcnt(7)
	v_or3_b32 v12, v56, v57, v58
	v_or_b32_e32 v12, v12, v59
	v_cmp_ne_u32_e32 vcc, 0, v12
	s_cbranch_vccnz .Lk1_hitm_7
.Lk1_contm_7:
	global_load_dwordx4 v[56:59], v1, s[6:7] nt
	s_add_u32 s6, s6, 0x400
	s_addc_u32 s7, s7, 0
	s_add_u32 s18, s18, 0x800
	s_sub_u32 s26, s26, 1
	s_cmp_lg_u32 s26, 1
	s_cbranch_scc1 .Lk1_main
	s_waitcnt vmcnt(7)
	v_or3_b32 v12, v28, v29, v30
	v_or_b32_e32 v12, v12, v31
	v_cmp_ne_u32_e32 vcc, 0, v12
	s_cbranch_vccnz .Lk1_hitl_0
.Lk1_contl_0:
	s_waitcnt vmcnt(6)
	v_or3_b32 v12, v32, v33, v34
	v_or_b32_e32 v12, v12, v35
	v_cmp_ne_u32_e32 vcc, 0, v12
	s_cbranch_vccnz .Lk1_hitl_1
.Lk1_contl_1:
	s_waitcnt vmcnt(5)
	v_or3_b32 v12, v36, v37, v38
	v_or_b32_e32 v12, v12, v39
	v_cmp_ne_u32_e32 vcc, 0, v12
	s_cbranch_vccnz .Lk1_hitl_2
.Lk1_contl_2:
	s_waitcnt vmcnt(4)
	v_or3_b32 v12, v40, v41, v42
	v_or_b32_e32 v12, v12, v43
	v_cmp_ne_u32_e32 vcc, 0, v12
	s_cbranch_vccnz .Lk1_hitl_3
.Lk1_contl_3:
	s_waitcnt vmcnt(3)
	v_or3_b32 v12, v44, v45, v46
	v_or_b32_e32 v12, v12, v47
	v_cmp_ne_u32_e32 vcc, 0, v12
	s_cbranch_vccnz .Lk1_hitl_4
.Lk1_contl_4:
	s_waitcnt vmcnt(2)
	v_or3_b32 v12, v48, v49, v50
	v_or_b32_e32 v12, v12, v51
	v_cmp_ne_u32_e32 vcc, 0, v12
	s_cbranch_vccnz .Lk1_hitl_5
.Lk1_contl_5:
	s_waitcnt vmcnt(1)
	v_or3_b32 v12, v52, v53, v54
	v_or_b32_e32 v12, v12, v55
	v_cmp_ne_u32_e32 vcc, 0, v12
	s_cbranch_vccnz .Lk1_hitl_6
.Lk1_contl_6:
	s_waitcnt vmcnt(0)
	v_or3_b32 v12, v56, v57, v58
	v_or_b32_e32 v12, v12, v59
	v_cmp_ne_u32_e32 vcc, 0, v12
	s_cbranch_vccnz .Lk1_hitl_7

.Lk1_cskip_fin_pend:
	s_mov_b64 s[40:41], 0
	s_mov_b64 s[42:43], 0
	s_mov_b64 s[44:45], 0
	s_mov_b64 s[46:47], 0
	s_cmp_ge_u32 s28, s25
	s_cbranch_scc1 .Lk1_inone_fin0
	s_waitcnt lgkmcnt(0)
	v_lshl_add_u32 v25, v6, 3, s28
	v_cmp_gt_u32_e32 vcc, s25, v25
	s_and_saveexec_b64 s[32:33], vcc
	s_mov_b64 s[40:41], exec
	ds_read_b64 v[28:29], v25
	s_waitcnt lgkmcnt(0)
	v_lshrrev_b32_e32 v33, 12, v28
	v_mul_hi_u32 v33, v33, s29
	v_mul_u32_u24_e32 v30, 0x3000, v33
	v_sub_u32_e32 v30, v28, v30
	v_lshlrev_b32_e32 v31, 2, v30
	global_atomic_add v32, v31, v21, s[8:9] sc0
	global_atomic_add_f32 v31, v29, s[10:11]
	v_mov_b32_e32 v28, v33
	s_mov_b64 exec, -1
	s_add_u32 s28, s28, 0x200
.Lk1_inone_fin0:
	s_cmp_ge_u32 s28, s25
	s_cbranch_scc1 .Lk1_inone_fin1
	s_waitcnt lgkmcnt(0)
	v_lshl_add_u32 v25, v6, 3, s28
	v_cmp_gt_u32_e32 vcc, s25, v25
	s_and_saveexec_b64 s[32:33], vcc
	s_mov_b64 s[42:43], exec
	ds_read_b64 v[36:37], v25
	s_waitcnt lgkmcnt(0)
	v_lshrrev_b32_e32 v41, 12, v36
	v_mul_hi_u32 v41, v41, s29
	v_mul_u32_u24_e32 v38, 0x3000, v41
	v_sub_u32_e32 v38, v36, v38
	v_lshlrev_b32_e32 v39, 2, v38
	global_atomic_add v40, v39, v21, s[8:9] sc0
	global_atomic_add_f32 v39, v37, s[10:11]
	v_mov_b32_e32 v36, v41
	s_mov_b64 exec, -1
	s_add_u32 s28, s28, 0x200
.Lk1_inone_fin1:
	s_cmp_ge_u32 s28, s25
	s_cbranch_scc1 .Lk1_inone_fin2
	s_waitcnt lgkmcnt(0)
	v_lshl_add_u32 v25, v6, 3, s28
	v_cmp_gt_u32_e32 vcc, s25, v25
	s_and_saveexec_b64 s[32:33], vcc
	s_mov_b64 s[44:45], exec
	ds_read_b64 v[44:45], v25
	s_waitcnt lgkmcnt(0)
	v_lshrrev_b32_e32 v49, 12, v44
	v_mul_hi_u32 v49, v49, s29
	v_mul_u32_u24_e32 v46, 0x3000, v49
	v_sub_u32_e32 v46, v44, v46
	v_lshlrev_b32_e32 v47, 2, v46
	global_atomic_add v48, v47, v21, s[8:9] sc0
	global_atomic_add_f32 v47, v45, s[10:11]
	v_mov_b32_e32 v44, v49
	s_mov_b64 exec, -1
	s_add_u32 s28, s28, 0x200
.Lk1_inone_fin2:
	s_cmp_ge_u32 s28, s25
	s_cbranch_scc1 .Lk1_inone_fin3
	s_waitcnt lgkmcnt(0)
	v_lshl_add_u32 v25, v6, 3, s28
	v_cmp_gt_u32_e32 vcc, s25, v25
	s_and_saveexec_b64 s[32:33], vcc
	s_mov_b64 s[46:47], exec
	ds_read_b64 v[52:53], v25
	s_waitcnt lgkmcnt(0)
	v_lshrrev_b32_e32 v57, 12, v52
	v_mul_hi_u32 v57, v57, s29
	v_mul_u32_u24_e32 v54, 0x3000, v57
	v_sub_u32_e32 v54, v52, v54
	v_lshlrev_b32_e32 v55, 2, v54
	global_atomic_add v56, v55, v21, s[8:9] sc0
	global_atomic_add_f32 v55, v53, s[10:11]
	v_mov_b32_e32 v52, v57
	s_mov_b64 exec, -1
	s_add_u32 s28, s28, 0x200
.Lk1_inone_fin3:
	s_waitcnt vmcnt(0)
	s_mov_b64 exec, s[40:41]
	s_cbranch_execz .Lk1_cskip_finc0
	v_mul_u32_u24_e32 v34, 0x3000, v30
	v_lshlrev_b32_e32 v33, 6, v30
	v_cmp_gt_u32_e32 vcc, 64, v32
	v_add_u32_e32 v33, v33, v32
	v_add3_u32 v34, v34, v32, s31
	v_cndmask_b32_e32 v33, v34, v33, vcc
	v_lshlrev_b32_e32 v33, 3, v33
	global_store_dwordx2 v33, v[28:29], s[12:13]
.Lk1_cskip_finc0:
	s_mov_b64 exec, -1
	s_mov_b64 exec, s[42:43]
	s_cbranch_execz .Lk1_cskip_finc1
	v_mul_u32_u24_e32 v42, 0x3000, v38
	v_lshlrev_b32_e32 v41, 6, v38
	v_cmp_gt_u32_e32 vcc, 64, v40
	v_add_u32_e32 v41, v41, v40
	v_add3_u32 v42, v42, v40, s31
	v_cndmask_b32_e32 v41, v42, v41, vcc
	v_lshlrev_b32_e32 v41, 3, v41
	global_store_dwordx2 v41, v[36:37], s[12:13]
.Lk1_cskip_finc1:
	s_mov_b64 exec, -1
	s_mov_b64 exec, s[44:45]
	s_cbranch_execz .Lk1_cskip_finc2
	v_mul_u32_u24_e32 v50, 0x3000, v46
	v_lshlrev_b32_e32 v49, 6, v46
	v_cmp_gt_u32_e32 vcc, 64, v48
	v_add_u32_e32 v49, v49, v48
	v_add3_u32 v50, v50, v48, s31
	v_cndmask_b32_e32 v49, v50, v49, vcc
	v_lshlrev_b32_e32 v49, 3, v49
	global_store_dwordx2 v49, v[44:45], s[12:13]
.Lk1_cskip_finc2:
	s_mov_b64 exec, -1
	s_mov_b64 exec, s[46:47]
	s_cbranch_execz .Lk1_cskip_finc3
	v_mul_u32_u24_e32 v58, 0x3000, v54
	v_lshlrev_b32_e32 v57, 6, v54
	v_cmp_gt_u32_e32 vcc, 64, v56
	v_add_u32_e32 v57, v57, v56
	v_add3_u32 v58, v58, v56, s31
	v_cndmask_b32_e32 v57, v58, v57, vcc
	v_lshlrev_b32_e32 v57, 3, v57
	global_store_dwordx2 v57, v[52:53], s[12:13]
.Lk1_cskip_finc3:
	s_mov_b64 exec, -1
	s_cmp_lt_u32 s28, s25
	s_cbranch_scc1 .Lk1_final
	s_endpgm

.Lk1_hitl_0:
	v_mov_b32_e32 v8, v28
	v_mov_b32_e32 v9, v29
	v_mov_b32_e32 v10, v30
	v_mov_b32_e32 v11, v31
	s_mov_b32 s19, s18
	s_movk_i32 s23, 8
	s_branch .Lk1_slow
.Lk1_hitl_1:
	v_mov_b32_e32 v8, v32
	v_mov_b32_e32 v9, v33
	v_mov_b32_e32 v10, v34
	v_mov_b32_e32 v11, v35
	s_add_u32 s19, s18, 0x100
	s_movk_i32 s23, 9
	s_branch .Lk1_slow
.Lk1_hitl_2:
	v_mov_b32_e32 v8, v36
	v_mov_b32_e32 v9, v37
	v_mov_b32_e32 v10, v38
	v_mov_b32_e32 v11, v39
	s_add_u32 s19, s18, 0x200
	s_movk_i32 s23, 10
	s_branch .Lk1_slow
.Lk1_hitl_3:
	v_mov_b32_e32 v8, v40
	v_mov_b32_e32 v9, v41
	v_mov_b32_e32 v10, v42
	v_mov_b32_e32 v11, v43
	s_add_u32 s19, s18, 0x300
	s_movk_i32 s23, 11
	s_branch .Lk1_slow
.Lk1_hitl_4:
	v_mov_b32_e32 v8, v44
	v_mov_b32_e32 v9, v45
	v_mov_b32_e32 v10, v46
	v_mov_b32_e32 v11, v47
	s_add_u32 s19, s18, 0x400
	s_movk_i32 s23, 12
	s_branch .Lk1_slow
.Lk1_hitl_5:
	v_mov_b32_e32 v8, v48
	v_mov_b32_e32 v9, v49
	v_mov_b32_e32 v10, v50
	v_mov_b32_e32 v11, v51
	s_add_u32 s19, s18, 0x500
	s_movk_i32 s23, 13
	s_branch .Lk1_slow
.Lk1_hitl_6:
	v_mov_b32_e32 v8, v52
	v_mov_b32_e32 v9, v53
	v_mov_b32_e32 v10, v54
	v_mov_b32_e32 v11, v55
	s_add_u32 s19, s18, 0x600
	s_movk_i32 s23, 14
	s_branch .Lk1_slow
.Lk1_hitl_7:
	v_mov_b32_e32 v8, v56
	v_mov_b32_e32 v9, v57
	v_mov_b32_e32 v10, v58
	v_mov_b32_e32 v11, v59
	s_add_u32 s19, s18, 0x700
	s_movk_i32 s23, 15
	s_branch .Lk1_slow

.Lk1_sk3:
	s_sub_u32 s22, s25, s24
	s_cmp_gt_u32 s22, 0x1800
	s_cbranch_scc1 .Lk1_flush
.Lk1_disp:
	s_cmp_lt_u32 s23, 8
	s_cbranch_scc1 .Lk1_d1
	s_cmp_lt_u32 s23, 12
	s_cbranch_scc1 .Lk1_d2
	s_cmp_lt_u32 s23, 14
	s_cbranch_scc1 .Lk1_d3
	s_cmp_lt_u32 s23, 15
	s_cbranch_scc1 .Lk1_d4
	s_branch .Lk1_contl_7

.Lk1_cskip_f:
	s_cmp_ge_u32 s28, s25
	s_cbranch_scc1 .Lk1_fdone
	s_cmp_ge_u32 s28, s25
	s_cbranch_scc1 .Lk1_inone_f
	s_waitcnt lgkmcnt(0)
	v_lshl_add_u32 v25, v6, 3, s28
	v_cmp_gt_u32_e32 vcc, s25, v25
	s_and_saveexec_b64 s[32:33], vcc
	s_mov_b64 s[34:35], exec
	ds_read_b64 v[16:17], v25
	s_waitcnt lgkmcnt(0)
	v_lshrrev_b32_e32 v23, 12, v16
	v_mul_hi_u32 v23, v23, s29
	v_mul_u32_u24_e32 v19, 0x3000, v23
	v_sub_u32_e32 v19, v16, v19
	v_lshlrev_b32_e32 v20, 2, v19
	global_atomic_add v22, v20, v21, s[8:9] sc0
	global_atomic_add_f32 v20, v17, s[10:11]
	v_mov_b32_e32 v16, v23
	s_mov_b64 exec, -1
	s_mov_b32 s36, 1
	s_add_u32 s28, s28, 0x200
	s_cmp_ge_u32 s28, s25
	s_cbranch_scc0 .Lk1_inone_f
	s_mov_b32 s28, s24
	s_mov_b32 s25, s24

	.amdhsa_kernel _Z9k1_kernelPKfS0_S0_PDF16_PiPfP15HIP_vector_typeIiLj2EES6_
		.amdhsa_group_segment_fixed_size 37392
		.amdhsa_private_segment_fixed_size 0
		.amdhsa_kernarg_size 64
		.amdhsa_user_sgpr_count 2
		.amdhsa_user_sgpr_dispatch_ptr 0
		.amdhsa_user_sgpr_queue_ptr 0
		.amdhsa_user_sgpr_kernarg_segment_ptr 1
		.amdhsa_user_sgpr_dispatch_id 0
		.amdhsa_user_sgpr_kernarg_preload_length 0
		.amdhsa_user_sgpr_kernarg_preload_offset 0
		.amdhsa_user_sgpr_private_segment_size 0
		.amdhsa_uses_dynamic_stack 0
		.amdhsa_enable_private_segment 0
		.amdhsa_system_sgpr_workgroup_id_x 1
		.amdhsa_system_sgpr_workgroup_id_y 0
		.amdhsa_system_sgpr_workgroup_id_z 0
		.amdhsa_system_sgpr_workgroup_info 0
		.amdhsa_system_vgpr_workitem_id 0
		.amdhsa_next_free_vgpr 140
		.amdhsa_next_free_sgpr 96
		.amdhsa_accum_offset 140
		.amdhsa_reserve_vcc 1
		.amdhsa_float_round_mode_32 0
		.amdhsa_float_round_mode_16_64 0
		.amdhsa_float_denorm_mode_32 3
		.amdhsa_float_denorm_mode_16_64 3
		.amdhsa_dx10_clamp 1
		.amdhsa_ieee_mode 1
		.amdhsa_fp16_overflow 0
		.amdhsa_tg_split 0
		.amdhsa_exception_fp_ieee_invalid_op 0
		.amdhsa_exception_fp_denorm_src 0
		.amdhsa_exception_fp_ieee_div_zero 0
		.amdhsa_exception_fp_ieee_overflow 0
		.amdhsa_exception_fp_ieee_underflow 0
		.amdhsa_exception_fp_ieee_inexact 0
		.amdhsa_exception_int_div_zero 0
	.end_amdhsa_kernel

.Lfunc_end0:
	.size	_Z9k1_kernelPKfS0_S0_PDF16_PiPfP15HIP_vector_typeIiLj2EES6_, .Lfunc_end0-_Z9k1_kernelPKfS0_S0_PDF16_PiPfP15HIP_vector_typeIiLj2EES6_
	.set _Z9k1_kernelPKfS0_S0_PDF16_PiPfP15HIP_vector_typeIiLj2EES6_.num_vgpr, 140
	.set _Z9k1_kernelPKfS0_S0_PDF16_PiPfP15HIP_vector_typeIiLj2EES6_.num_agpr, 0
	.set _Z9k1_kernelPKfS0_S0_PDF16_PiPfP15HIP_vector_typeIiLj2EES6_.numbered_sgpr, 26
	.set _Z9k1_kernelPKfS0_S0_PDF16_PiPfP15HIP_vector_typeIiLj2EES6_.num_named_barrier, 0
	.set _Z9k1_kernelPKfS0_S0_PDF16_PiPfP15HIP_vector_typeIiLj2EES6_.private_seg_size, 0
	.set _Z9k1_kernelPKfS0_S0_PDF16_PiPfP15HIP_vector_typeIiLj2EES6_.uses_vcc, 1
	.set _Z9k1_kernelPKfS0_S0_PDF16_PiPfP15HIP_vector_typeIiLj2EES6_.uses_flat_scratch, 0
	.set _Z9k1_kernelPKfS0_S0_PDF16_PiPfP15HIP_vector_typeIiLj2EES6_.has_dyn_sized_stack, 0
	.set _Z9k1_kernelPKfS0_S0_PDF16_PiPfP15HIP_vector_typeIiLj2EES6_.has_recursion, 0
	.set _Z9k1_kernelPKfS0_S0_PDF16_PiPfP15HIP_vector_typeIiLj2EES6_.has_indirect_call, 0

amdhsa.kernels:
  - .agpr_count:     0
    .args:
      - .actual_access:  read_only
        .address_space:  global
        .offset:         0
        .size:           8
        .value_kind:     global_buffer
      - .actual_access:  read_only
        .address_space:  global
        .offset:         8
        .size:           8
        .value_kind:     global_buffer
      - .actual_access:  read_only
        .address_space:  global
        .offset:         16
        .size:           8
        .value_kind:     global_buffer
      - .actual_access:  write_only
        .address_space:  global
        .offset:         24
        .size:           8
        .value_kind:     global_buffer
      - .address_space:  global
        .offset:         32
        .size:           8
        .value_kind:     global_buffer
      - .address_space:  global
        .offset:         40
        .size:           8
        .value_kind:     global_buffer
      - .actual_access:  write_only
        .address_space:  global
        .offset:         48
        .size:           8
        .value_kind:     global_buffer
      - .actual_access:  write_only
        .address_space:  global
        .offset:         56
        .size:           8
        .value_kind:     global_buffer
    .group_segment_fixed_size: 37392
    .kernarg_segment_align: 8
    .kernarg_segment_size: 64
    .language:       OpenCL C
    .language_version:
      - 2
      - 0
    .max_flat_workgroup_size: 256
    .name:           _Z9k1_kernelPKfS0_S0_PDF16_PiPfP15HIP_vector_typeIiLj2EES6_
    .private_segment_fixed_size: 0
    .sgpr_count:     32
    .sgpr_spill_count: 0
    .symbol:         _Z9k1_kernelPKfS0_S0_PDF16_PiPfP15HIP_vector_typeIiLj2EES6_.kd
    .uniform_work_group_size: 1
    .uses_dynamic_stack: false
    .vgpr_count:     140
    .vgpr_spill_count: 0
    .wavefront_size: 64
  - .agpr_count:     0
    .args:
      - .actual_access:  read_only
        .address_space:  global
        .offset:         0
        .size:           8
        .value_kind:     global_buffer
      - .actual_access:  read_only
        .address_space:  global
        .offset:         8
        .size:           8
        .value_kind:     global_buffer
      - .actual_access:  read_only
        .address_space:  global
        .offset:         16
        .size:           8
        .value_kind:     global_buffer
      - .actual_access:  read_only
        .address_space:  global
        .offset:         24
        .size:           8
        .value_kind:     global_buffer
      - .actual_access:  read_only
        .address_space:  global
        .offset:         32
        .size:           8
        .value_kind:     global_buffer
      - .actual_access:  read_only
        .address_space:  global
        .offset:         40
        .size:           8
        .value_kind:     global_buffer
      - .actual_access:  read_only
        .address_space:  global
        .offset:         48
        .size:           8
        .value_kind:     global_buffer
      - .actual_access:  read_only
        .address_space:  global
        .offset:         56
        .size:           8
        .value_kind:     global_buffer
      - .actual_access:  read_only
        .address_space:  global
        .offset:         64
        .size:           8
        .value_kind:     global_buffer
      - .actual_access:  write_only
        .address_space:  global
        .offset:         72
        .size:           8
        .value_kind:     global_buffer
      - .address_space:  global
        .offset:         80
        .size:           8
        .value_kind:     global_buffer
    .group_segment_fixed_size: 44224
    .kernarg_segment_align: 8
    .kernarg_segment_size: 88
    .language:       OpenCL C
    .language_version:
      - 2
      - 0
    .max_flat_workgroup_size: 512
    .name:           _Z11agg2_kernelPKiPKfPK15HIP_vector_typeIiLj2EEPKDF16_S2_S2_S2_S2_S2_PfS9_
    .private_segment_fixed_size: 0
    .sgpr_count:     41
    .sgpr_spill_count: 0
    .symbol:         _Z11agg2_kernelPKiPKfPK15HIP_vector_typeIiLj2EEPKDF16_S2_S2_S2_S2_S2_PfS9_.kd
    .uniform_work_group_size: 1
    .uses_dynamic_stack: false
    .vgpr_count:     80
    .vgpr_spill_count: 0
    .wavefront_size: 64
  - .agpr_count:     0
    .args:
      - .actual_access:  read_only
        .address_space:  global
        .offset:         0
        .size:           8
        .value_kind:     global_buffer
      - .actual_access:  read_only
        .address_space:  global
        .offset:         8
        .size:           8
        .value_kind:     global_buffer
      - .actual_access:  read_only
        .address_space:  global
        .offset:         16
        .size:           8
        .value_kind:     global_buffer
      - .actual_access:  read_only
        .address_space:  global
        .offset:         24
        .size:           8
        .value_kind:     global_buffer
      - .actual_access:  write_only
        .address_space:  global
        .offset:         32
        .size:           8
        .value_kind:     global_buffer
      - .offset:         40
        .size:           4
        .value_kind:     hidden_block_count_x
      - .offset:         44
        .size:           4
        .value_kind:     hidden_block_count_y
      - .offset:         48
        .size:           4
        .value_kind:     hidden_block_count_z
      - .offset:         52
        .size:           2
        .value_kind:     hidden_group_size_x
      - .offset:         54
        .size:           2
        .value_kind:     hidden_group_size_y
      - .offset:         56
        .size:           2
        .value_kind:     hidden_group_size_z
      - .offset:         58
        .size:           2
        .value_kind:     hidden_remainder_x
      - .offset:         60
        .size:           2
        .value_kind:     hidden_remainder_y
      - .offset:         62
        .size:           2
        .value_kind:     hidden_remainder_z
      - .offset:         80
        .size:           8
        .value_kind:     hidden_global_offset_x
      - .offset:         88
        .size:           8
        .value_kind:     hidden_global_offset_y
      - .offset:         96
        .size:           8
        .value_kind:     hidden_global_offset_z
      - .offset:         104
        .size:           2
        .value_kind:     hidden_grid_dims
    .group_segment_fixed_size: 512
    .kernarg_segment_align: 8
    .kernarg_segment_size: 296
    .language:       OpenCL C
    .language_version:
      - 2
      - 0
    .max_flat_workgroup_size: 256
    .name:           _Z12final_kernelPKfS0_S0_S0_Pf
    .private_segment_fixed_size: 0
    .sgpr_count:     18
    .sgpr_spill_count: 0
    .symbol:         _Z12final_kernelPKfS0_S0_S0_Pf.kd
    .uniform_work_group_size: 1
    .uses_dynamic_stack: false
    .vgpr_count:     36
    .vgpr_spill_count: 0
    .wavefront_size: 64
  - .agpr_count:     0
    .args:
      - .actual_access:  read_only
        .address_space:  global
        .offset:         0
        .size:           8
        .value_kind:     global_buffer
      - .actual_access:  read_only
        .address_space:  global
        .offset:         8
        .size:           8
        .value_kind:     global_buffer
      - .address_space:  global
        .offset:         16
        .size:           8
        .value_kind:     global_buffer
      - .address_space:  global
        .offset:         24
        .size:           8
        .value_kind:     global_buffer
      - .actual_access:  read_only
        .address_space:  global
        .offset:         32
        .size:           8
        .value_kind:     global_buffer
      - .actual_access:  read_only
        .address_space:  global
        .offset:         40
        .size:           8
        .value_kind:     global_buffer
      - .actual_access:  write_only
        .address_space:  global
        .offset:         48
        .size:           8
        .value_kind:     global_buffer
      - .address_space:  global
        .offset:         56
        .size:           8
        .value_kind:     global_buffer
    .group_segment_fixed_size: 8192
    .kernarg_segment_align: 8
    .kernarg_segment_size: 64
    .language:       OpenCL C
    .language_version:
      - 2
      - 0
    .max_flat_workgroup_size: 512
    .name:           _Z10agg_kernelILi128ELb1EEvPKiPKfP15HIP_vector_typeIiLj2EES6_PKDF16_S3_PDF16_Pf
    .private_segment_fixed_size: 0
    .sgpr_count:     42
    .sgpr_spill_count: 0
    .symbol:         _Z10agg_kernelILi128ELb1EEvPKiPKfP15HIP_vector_typeIiLj2EES6_PKDF16_S3_PDF16_Pf.kd
    .uniform_work_group_size: 1
    .uses_dynamic_stack: false
    .vgpr_count:     80
    .vgpr_spill_count: 0
    .wavefront_size: 64
